# baseline (speedup 1.0000x reference)
.Lpst3_join:
	s_add_i32 s36, s36, 2
	s_add_u32 s11, s11, 0xc000
	s_addc_u32 s35, s35, 0
	s_add_u32 s2, s2, 0xc000
	s_addc_u32 s3, s3, 0
	s_add_u32 s72, s72, 0xc000
	s_addc_u32 s73, s73, 0
	s_cmp_lt_u32 s36, 4
	v_mfma_scale_f32_16x16x128_f8f6f4 v[80:83], v[46:51], v[40:45], v[80:83], v187, v187 op_sel_hi:[0,0,0] cbsz:2 blgp:2
	v_mfma_scale_f32_16x16x128_f8f6f4 v[72:75], v[194:199], v[40:45], v[72:75], v187, v187 op_sel_hi:[0,0,0] cbsz:2 blgp:2
	v_mfma_scale_f32_16x16x128_f8f6f4 v[64:67], v[200:205], v[40:45], v[64:67], v187, v187 op_sel_hi:[0,0,0] cbsz:2 blgp:2
	v_mfma_scale_f32_16x16x128_f8f6f4 v[56:59], v[206:211], v[40:45], v[56:59], v187, v187 op_sel_hi:[0,0,0] cbsz:2 blgp:2
	v_mfma_scale_f32_16x16x128_f8f6f4 v[52:55], v[46:51], v[188:193], v[52:55], v187, v187 op_sel_hi:[0,0,0] cbsz:2 blgp:2
	v_mfma_scale_f32_16x16x128_f8f6f4 v[48:51], v[194:199], v[188:193], v[224:227], v187, v187 op_sel_hi:[0,0,0] cbsz:2 blgp:2
	v_mfma_scale_f32_16x16x128_f8f6f4 v[44:47], v[200:205], v[188:193], v[212:215], v187, v187 op_sel_hi:[0,0,0] cbsz:2 blgp:2
	v_mfma_scale_f32_16x16x128_f8f6f4 v[40:43], v[206:211], v[188:193], v[216:219], v187, v187 op_sel_hi:[0,0,0] cbsz:2 blgp:2
	s_waitcnt lgkmcnt(0)

.Lst3_join:
	s_add_i32 s36, s36, 2
	s_add_u32 s11, s11, 0xc000
	s_addc_u32 s35, s35, 0
	s_add_u32 s2, s2, 0xc000
	s_addc_u32 s3, s3, 0
	s_add_u32 s72, s72, 0xc000
	s_addc_u32 s73, s73, 0
	s_cmp_lt_u32 s36, 4
	v_mfma_scale_f32_16x16x128_f8f6f4 v[80:83], v[46:51], v[40:45], v[80:83], v187, v187 op_sel_hi:[0,0,0] cbsz:2 blgp:2
	v_mfma_scale_f32_16x16x128_f8f6f4 v[72:75], v[194:199], v[40:45], v[72:75], v187, v187 op_sel_hi:[0,0,0] cbsz:2 blgp:2
	v_mfma_scale_f32_16x16x128_f8f6f4 v[64:67], v[200:205], v[40:45], v[64:67], v187, v187 op_sel_hi:[0,0,0] cbsz:2 blgp:2
	v_mfma_scale_f32_16x16x128_f8f6f4 v[56:59], v[206:211], v[40:45], v[56:59], v187, v187 op_sel_hi:[0,0,0] cbsz:2 blgp:2
	v_mfma_scale_f32_16x16x128_f8f6f4 v[52:55], v[46:51], v[188:193], v[52:55], v187, v187 op_sel_hi:[0,0,0] cbsz:2 blgp:2
	v_mfma_scale_f32_16x16x128_f8f6f4 v[48:51], v[194:199], v[188:193], v[224:227], v187, v187 op_sel_hi:[0,0,0] cbsz:2 blgp:2
	v_mfma_scale_f32_16x16x128_f8f6f4 v[44:47], v[200:205], v[188:193], v[212:215], v187, v187 op_sel_hi:[0,0,0] cbsz:2 blgp:2
	v_mfma_scale_f32_16x16x128_f8f6f4 v[40:43], v[206:211], v[188:193], v[216:219], v187, v187 op_sel_hi:[0,0,0] cbsz:2 blgp:2
	s_waitcnt lgkmcnt(0)
	s_cbranch_scc1 .LBB1_3
